# GDN chain loader: four register stages (loads issued 5 steps ahead instead of 4), nt loads
# speedup vs baseline: 1.0046x; 1.0006x over previous
; #define LDS_BARRIER() asm volatile("s_waitcnt lgkmcnt(0)\n\ts_barrier" ::: "memory")
; __device__ void phase_gdn_chain(const Params& p, int l, char* smem, int vb, int nvb, int oz) {
;     ...
;             GDN_LOAD(ra, va, ga, 0)
;             GDN_LOAD(rb, vb_, gb, 1)
;             GDN_LOAD(rc, vc_, gc, 2)
;             GDN_FILL(ra, va, ga, 0)
;             GDN_LOAD(ra, va, ga, 3)
;             LDS_BARRIER();
;             for (int ci = 0; ci < 36; ci += 6) {
;                 GDN_FILL(rb, vb_, gb, 1)  if (ci + 4 < 36) GDN_LOAD(rb, vb_, gb, ci + 4)  LDS_BARRIER();
;                 GDN_FILL(rc, vc_, gc, 0)  if (ci + 5 < 36) GDN_LOAD(rc, vc_, gc, ci + 5)  LDS_BARRIER();
;                 GDN_FILL(ra, va, ga, 1)  if (ci + 6 < 36) GDN_LOAD(ra, va, ga, ci + 6)  LDS_BARRIER();
;                 GDN_FILL(rb, vb_, gb, 0)  if (ci + 7 < 36) GDN_LOAD(rb, vb_, gb, ci + 7)  LDS_BARRIER();
;                 GDN_FILL(rc, vc_, gc, 1)  if (ci + 8 < 36) GDN_LOAD(rc, vc_, gc, ci + 8)  LDS_BARRIER();
;                 if (ci + 6 < 36) GDN_FILL(ra, va, ga, 0)  if (ci + 9 < 36) GDN_LOAD(ra, va, ga, ci + 9)  LDS_BARRIER();
;             }
.LBB0_439:
	s_or_b64 exec, exec, s[46:47]
	s_and_b64 s[26:27], s[44:45], exec
	s_cselect_b32 s25, 4, 35
	s_add_i32 s26, s25, s2
	s_ashr_i32 s27, s26, 31
	s_add_u32 s42, s26, s84
	s_addc_u32 s43, s27, 0
	s_lshl_b64 s[46:47], s[42:43], 13
	s_add_u32 s48, s4, s46
	s_addc_u32 s49, s5, s47
	s_add_u32 s50, s6, s46
	s_addc_u32 s51, s7, s47
	s_lshl_b64 s[26:27], s[26:27], 13
	s_add_u32 s52, s8, s26
	s_addc_u32 s53, s9, s27
	s_add_u32 s26, s10, s26
	s_addc_u32 s27, s11, s27
	s_add_u32 s46, s12, s46
	s_addc_u32 s47, s13, s47
	global_load_dwordx4 v[4:7], v2, s[48:49] nt
	global_load_dwordx4 v[12:15], v2, s[50:51] nt
	global_load_dwordx4 v[16:19], v215, s[50:51] nt
	global_load_dwordx4 v[24:27], v215, s[52:53] nt
	global_load_dwordx4 v[20:23], v2, s[52:53] nt
	global_load_dwordx4 v[28:31], v2, s[26:27] nt
	global_load_dwordx4 v[8:11], v215, s[48:49] nt
	global_load_dwordx4 v[36:39], v2, s[46:47] nt
	global_load_dwordx4 v[32:35], v215, s[26:27] nt
	global_load_dwordx4 v[40:43], v215, s[46:47] nt
	s_lshl_b64 s[26:27], s[42:43], 10
	s_add_u32 s42, s14, s26
	s_addc_u32 s43, s15, s27
	s_and_saveexec_b64 s[46:47], s[38:39]
	s_cbranch_execz .Lg4_la1
	global_load_dword v44, v216, s[42:43]
.Lg4_la1:
	s_or_b64 exec, exec, s[46:47]
	s_and_saveexec_b64 s[46:47], s[40:41]
	s_cbranch_execz .Lg4_lb1
	global_load_dword v45, v3, s[42:43] offset:512
.Lg4_lb1:
	s_or_b64 exec, exec, s[46:47]
	s_waitcnt lgkmcnt(0)
	s_barrier
	s_mov_b32 s3, 0
	v_add_u32_e32 v224, 0x11e10, v223
	v_add_u32_e32 v225, 0x14210, v193
.Lg4_loop:
	s_cmp_lt_u32 s3, 32
	s_cbranch_scc1 .Lg4_w30_0
	s_waitcnt vmcnt(20)
	s_branch .Lg4_wd_0
.Lg4_w30_0:
	s_waitcnt vmcnt(30)
.Lg4_wd_0:
	ds_write_b128 v223, v[68:71] offset:45584
	ds_write_b128 v223, v[96:99] offset:50192
	ds_write_b128 v223, v[72:75] offset:54800
	ds_write_b128 v223, v[76:79] offset:59408
	ds_write_b128 v223, v[88:91] offset:64016
	ds_write_b128 v214, v[80:83] offset:64016
	ds_write_b128 v224, v[84:87]
	ds_write_b128 v224, v[104:107] offset:4608
	ds_write_b128 v225, v[92:95]
	ds_write_b128 v225, v[100:103] offset:4096
	s_and_saveexec_b64 s[42:43], s[38:39]
	s_cbranch_execz .Lg4_fa2
	ds_write_b32 v195, v220
.Lg4_fa2:
	s_or_b64 exec, exec, s[42:43]
	s_and_saveexec_b64 s[42:43], s[40:41]
	s_cbranch_execz .Lg4_fb2
	v_readlane_b32 s17, v255, 40
	s_nop 1
	v_mov_b32_e32 v226, s17
	ds_write_b32 v226, v219
.Lg4_fb2:
	s_or_b64 exec, exec, s[42:43]
	s_cmp_gt_u32 s3, 30
	s_cbranch_scc1 .Lg4_nold_0
	s_add_i32 s25, s3, 5
	s_sub_i32 s31, 34, s3
	s_and_b64 s[26:27], s[44:45], exec
	s_cselect_b32 s25, s25, s31
	s_add_i32 s26, s25, s2
	s_ashr_i32 s27, s26, 31
	s_add_u32 s42, s26, s84
	s_addc_u32 s43, s27, 0
	s_lshl_b64 s[46:47], s[42:43], 13
	s_add_u32 s48, s4, s46
	s_addc_u32 s49, s5, s47
	s_add_u32 s50, s6, s46
	s_addc_u32 s51, s7, s47
	s_lshl_b64 s[26:27], s[26:27], 13
	s_add_u32 s52, s8, s26
	s_addc_u32 s53, s9, s27
	s_add_u32 s26, s10, s26
	s_addc_u32 s27, s11, s27
	s_add_u32 s46, s12, s46
	s_addc_u32 s47, s13, s47
	global_load_dwordx4 v[68:71], v2, s[48:49] nt
	global_load_dwordx4 v[72:75], v2, s[50:51] nt
	global_load_dwordx4 v[76:79], v215, s[50:51] nt
	global_load_dwordx4 v[80:83], v215, s[52:53] nt
	global_load_dwordx4 v[88:91], v2, s[52:53] nt
	global_load_dwordx4 v[84:87], v2, s[26:27] nt
	global_load_dwordx4 v[96:99], v215, s[48:49] nt
	global_load_dwordx4 v[92:95], v2, s[46:47] nt
	global_load_dwordx4 v[104:107], v215, s[26:27] nt
	global_load_dwordx4 v[100:103], v215, s[46:47] nt
	s_lshl_b64 s[26:27], s[42:43], 10
	s_add_u32 s42, s14, s26
	s_addc_u32 s43, s15, s27
	s_and_saveexec_b64 s[46:47], s[38:39]
	s_cbranch_execz .Lg4_la3
	global_load_dword v220, v216, s[42:43]

; #define LDS_BARRIER() asm volatile("s_waitcnt lgkmcnt(0)\n\ts_barrier" ::: "memory")
; __device__ void phase_gdn_chain(const Params& p, int l, char* smem, int vb, int nvb, int oz) {
;     ...
;             for (int ci = 0; ci < 36; ci += 6) {
;                 GDN_FILL(rb, vb_, gb, 1)  if (ci + 4 < 36) GDN_LOAD(rb, vb_, gb, ci + 4)  LDS_BARRIER();
;                 GDN_FILL(rc, vc_, gc, 0)  if (ci + 5 < 36) GDN_LOAD(rc, vc_, gc, ci + 5)  LDS_BARRIER();
;                 GDN_FILL(ra, va, ga, 1)  if (ci + 6 < 36) GDN_LOAD(ra, va, ga, ci + 6)  LDS_BARRIER();
;                 GDN_FILL(rb, vb_, gb, 0)  if (ci + 7 < 36) GDN_LOAD(rb, vb_, gb, ci + 7)  LDS_BARRIER();
;                 GDN_FILL(rc, vc_, gc, 1)  if (ci + 8 < 36) GDN_LOAD(rc, vc_, gc, ci + 8)  LDS_BARRIER();
;                 if (ci + 6 < 36) GDN_FILL(ra, va, ga, 0)  if (ci + 9 < 36) GDN_LOAD(ra, va, ga, ci + 9)  LDS_BARRIER();
;             }
.Lg4_nold_0:
	s_waitcnt lgkmcnt(0)
	s_barrier
	s_cmp_lt_u32 s3, 32
	s_cbranch_scc1 .Lg4_w30_1
	s_waitcnt vmcnt(10)
	s_branch .Lg4_wd_1

; #define LDS_BARRIER() asm volatile("s_waitcnt lgkmcnt(0)\n\ts_barrier" ::: "memory")
; __device__ void phase_gdn_chain(const Params& p, int l, char* smem, int vb, int nvb, int oz) {
;     ...
;             for (int ci = 0; ci < 36; ci += 6) {
;                 GDN_FILL(rb, vb_, gb, 1)  if (ci + 4 < 36) GDN_LOAD(rb, vb_, gb, ci + 4)  LDS_BARRIER();
;                 GDN_FILL(rc, vc_, gc, 0)  if (ci + 5 < 36) GDN_LOAD(rc, vc_, gc, ci + 5)  LDS_BARRIER();
;                 GDN_FILL(ra, va, ga, 1)  if (ci + 6 < 36) GDN_LOAD(ra, va, ga, ci + 6)  LDS_BARRIER();
;                 GDN_FILL(rb, vb_, gb, 0)  if (ci + 7 < 36) GDN_LOAD(rb, vb_, gb, ci + 7)  LDS_BARRIER();
;                 GDN_FILL(rc, vc_, gc, 1)  if (ci + 8 < 36) GDN_LOAD(rc, vc_, gc, ci + 8)  LDS_BARRIER();
;                 if (ci + 6 < 36) GDN_FILL(ra, va, ga, 0)  if (ci + 9 < 36) GDN_LOAD(ra, va, ga, ci + 9)  LDS_BARRIER();
;             }
.Lg4_wd_1:
	ds_write_b128 v223, v[108:111]
	ds_write_b128 v223, v[136:139] offset:4608
	ds_write_b128 v223, v[112:115] offset:9216
	ds_write_b128 v223, v[116:119] offset:13824
	ds_write_b128 v223, v[124:127] offset:18432
	ds_write_b128 v223, v[120:123] offset:23040
	ds_write_b128 v223, v[128:131] offset:27648
	ds_write_b128 v223, v[140:143] offset:32256
	ds_write_b128 v193, v[132:135] offset:36864
	ds_write_b128 v193, v[144:147] offset:40960
	s_and_saveexec_b64 s[42:43], s[38:39]
	s_cbranch_execz .Lg4_fa4
	ds_write_b32 v213, v222 offset:45056
.Lg4_fa4:
	s_or_b64 exec, exec, s[42:43]
	s_and_saveexec_b64 s[42:43], s[40:41]
	s_cbranch_execz .Lg4_fb4
	ds_write_b32 v3, v221 offset:45568
.Lg4_fb4:
	s_or_b64 exec, exec, s[42:43]
	s_cmp_gt_u32 s3, 29
	s_cbranch_scc1 .Lg4_nold_1
	s_add_i32 s25, s3, 6
	s_sub_i32 s31, 33, s3
	s_and_b64 s[26:27], s[44:45], exec
	s_cselect_b32 s25, s25, s31
	s_add_i32 s26, s25, s2
	s_ashr_i32 s27, s26, 31
	s_add_u32 s42, s26, s84
	s_addc_u32 s43, s27, 0
	s_lshl_b64 s[46:47], s[42:43], 13
	s_add_u32 s48, s4, s46
	s_addc_u32 s49, s5, s47
	s_add_u32 s50, s6, s46
	s_addc_u32 s51, s7, s47
	s_lshl_b64 s[26:27], s[26:27], 13
	s_add_u32 s52, s8, s26
	s_addc_u32 s53, s9, s27
	s_add_u32 s26, s10, s26
	s_addc_u32 s27, s11, s27
	s_add_u32 s46, s12, s46
	s_addc_u32 s47, s13, s47
	global_load_dwordx4 v[108:111], v2, s[48:49] nt
	global_load_dwordx4 v[112:115], v2, s[50:51] nt
	global_load_dwordx4 v[116:119], v215, s[50:51] nt
	global_load_dwordx4 v[120:123], v215, s[52:53] nt
	global_load_dwordx4 v[124:127], v2, s[52:53] nt
	global_load_dwordx4 v[128:131], v2, s[26:27] nt
	global_load_dwordx4 v[136:139], v215, s[48:49] nt
	global_load_dwordx4 v[132:135], v2, s[46:47] nt
	global_load_dwordx4 v[140:143], v215, s[26:27] nt
	global_load_dwordx4 v[144:147], v215, s[46:47] nt
	s_lshl_b64 s[26:27], s[42:43], 10
	s_add_u32 s42, s14, s26
	s_addc_u32 s43, s15, s27
	s_and_saveexec_b64 s[46:47], s[38:39]
	s_cbranch_execz .Lg4_la5
	global_load_dword v222, v216, s[42:43]

; #define LDS_BARRIER() asm volatile("s_waitcnt lgkmcnt(0)\n\ts_barrier" ::: "memory")
; __device__ void phase_gdn_chain(const Params& p, int l, char* smem, int vb, int nvb, int oz) {
;     ...
;             for (int ci = 0; ci < 36; ci += 6) {
;                 GDN_FILL(rb, vb_, gb, 1)  if (ci + 4 < 36) GDN_LOAD(rb, vb_, gb, ci + 4)  LDS_BARRIER();
;                 GDN_FILL(rc, vc_, gc, 0)  if (ci + 5 < 36) GDN_LOAD(rc, vc_, gc, ci + 5)  LDS_BARRIER();
;                 GDN_FILL(ra, va, ga, 1)  if (ci + 6 < 36) GDN_LOAD(ra, va, ga, ci + 6)  LDS_BARRIER();
;                 GDN_FILL(rb, vb_, gb, 0)  if (ci + 7 < 36) GDN_LOAD(rb, vb_, gb, ci + 7)  LDS_BARRIER();
;                 GDN_FILL(rc, vc_, gc, 1)  if (ci + 8 < 36) GDN_LOAD(rc, vc_, gc, ci + 8)  LDS_BARRIER();
;                 if (ci + 6 < 36) GDN_FILL(ra, va, ga, 0)  if (ci + 9 < 36) GDN_LOAD(ra, va, ga, ci + 9)  LDS_BARRIER();
;             }
.Lg4_nold_1:
	s_waitcnt lgkmcnt(0)
	s_barrier
	s_cmp_lt_u32 s3, 32
	s_cbranch_scc1 .Lg4_w30_2
	s_waitcnt vmcnt(0)
	s_branch .Lg4_wd_2

; #define LDS_BARRIER() asm volatile("s_waitcnt lgkmcnt(0)\n\ts_barrier" ::: "memory")
; __device__ void phase_gdn_chain(const Params& p, int l, char* smem, int vb, int nvb, int oz) {
;     ...
;             for (int ci = 0; ci < 36; ci += 6) {
;                 GDN_FILL(rb, vb_, gb, 1)  if (ci + 4 < 36) GDN_LOAD(rb, vb_, gb, ci + 4)  LDS_BARRIER();
;                 GDN_FILL(rc, vc_, gc, 0)  if (ci + 5 < 36) GDN_LOAD(rc, vc_, gc, ci + 5)  LDS_BARRIER();
;                 GDN_FILL(ra, va, ga, 1)  if (ci + 6 < 36) GDN_LOAD(ra, va, ga, ci + 6)  LDS_BARRIER();
;                 GDN_FILL(rb, vb_, gb, 0)  if (ci + 7 < 36) GDN_LOAD(rb, vb_, gb, ci + 7)  LDS_BARRIER();
;                 GDN_FILL(rc, vc_, gc, 1)  if (ci + 8 < 36) GDN_LOAD(rc, vc_, gc, ci + 8)  LDS_BARRIER();
;                 if (ci + 6 < 36) GDN_FILL(ra, va, ga, 0)  if (ci + 9 < 36) GDN_LOAD(ra, va, ga, ci + 9)  LDS_BARRIER();
;             }
.Lg4_wd_2:
	ds_write_b128 v223, v[148:151] offset:45584
	ds_write_b128 v223, v[172:175] offset:50192
	ds_write_b128 v223, v[152:155] offset:54800
	ds_write_b128 v223, v[156:159] offset:59408
	ds_write_b128 v223, v[164:167] offset:64016
	ds_write_b128 v214, v[160:163] offset:64016
	ds_write_b128 v224, v[168:171]
	ds_write_b128 v224, v[180:183] offset:4608
	ds_write_b128 v225, v[176:179]
	ds_write_b128 v225, v[184:187] offset:4096
	s_and_saveexec_b64 s[42:43], s[38:39]
	s_cbranch_execz .Lg4_fa6
	ds_write_b32 v195, v218
.Lg4_fa6:
	s_or_b64 exec, exec, s[42:43]
	s_and_saveexec_b64 s[42:43], s[40:41]
	s_cbranch_execz .Lg4_fb6
	v_readlane_b32 s17, v255, 40
	s_nop 1
	v_mov_b32_e32 v226, s17
	ds_write_b32 v226, v217
.Lg4_fb6:
	s_or_b64 exec, exec, s[42:43]
	s_cmp_gt_u32 s3, 28
	s_cbranch_scc1 .Lg4_nold_2
	s_add_i32 s25, s3, 7
	s_sub_i32 s31, 32, s3
	s_and_b64 s[26:27], s[44:45], exec
	s_cselect_b32 s25, s25, s31
	s_add_i32 s26, s25, s2
	s_ashr_i32 s27, s26, 31
	s_add_u32 s42, s26, s84
	s_addc_u32 s43, s27, 0
	s_lshl_b64 s[46:47], s[42:43], 13
	s_add_u32 s48, s4, s46
	s_addc_u32 s49, s5, s47
	s_add_u32 s50, s6, s46
	s_addc_u32 s51, s7, s47
	s_lshl_b64 s[26:27], s[26:27], 13
	s_add_u32 s52, s8, s26
	s_addc_u32 s53, s9, s27
	s_add_u32 s26, s10, s26
	s_addc_u32 s27, s11, s27
	s_add_u32 s46, s12, s46
	s_addc_u32 s47, s13, s47
	global_load_dwordx4 v[148:151], v2, s[48:49] nt
	global_load_dwordx4 v[152:155], v2, s[50:51] nt
	global_load_dwordx4 v[156:159], v215, s[50:51] nt
	global_load_dwordx4 v[160:163], v215, s[52:53] nt
	global_load_dwordx4 v[164:167], v2, s[52:53] nt
	global_load_dwordx4 v[168:171], v2, s[26:27] nt
	global_load_dwordx4 v[172:175], v215, s[48:49] nt
	global_load_dwordx4 v[176:179], v2, s[46:47] nt
	global_load_dwordx4 v[180:183], v215, s[26:27] nt
	global_load_dwordx4 v[184:187], v215, s[46:47] nt
	s_lshl_b64 s[26:27], s[42:43], 10
	s_add_u32 s42, s14, s26
	s_addc_u32 s43, s15, s27
	s_and_saveexec_b64 s[46:47], s[38:39]
	s_cbranch_execz .Lg4_la7
	global_load_dword v218, v216, s[42:43]

; #define LDS_BARRIER() asm volatile("s_waitcnt lgkmcnt(0)\n\ts_barrier" ::: "memory")
; __device__ void phase_gdn_chain(const Params& p, int l, char* smem, int vb, int nvb, int oz) {
;     ...
;             for (int ci = 0; ci < 36; ci += 6) {
;                 GDN_FILL(rb, vb_, gb, 1)  if (ci + 4 < 36) GDN_LOAD(rb, vb_, gb, ci + 4)  LDS_BARRIER();
;                 GDN_FILL(rc, vc_, gc, 0)  if (ci + 5 < 36) GDN_LOAD(rc, vc_, gc, ci + 5)  LDS_BARRIER();
;                 GDN_FILL(ra, va, ga, 1)  if (ci + 6 < 36) GDN_LOAD(ra, va, ga, ci + 6)  LDS_BARRIER();
;                 GDN_FILL(rb, vb_, gb, 0)  if (ci + 7 < 36) GDN_LOAD(rb, vb_, gb, ci + 7)  LDS_BARRIER();
;                 GDN_FILL(rc, vc_, gc, 1)  if (ci + 8 < 36) GDN_LOAD(rc, vc_, gc, ci + 8)  LDS_BARRIER();
;                 if (ci + 6 < 36) GDN_FILL(ra, va, ga, 0)  if (ci + 9 < 36) GDN_LOAD(ra, va, ga, ci + 9)  LDS_BARRIER();
;             }
.Lg4_nold_2:
	s_waitcnt lgkmcnt(0)
	s_barrier
	s_cmp_lt_u32 s3, 32
	s_cbranch_scc0 .Lg4_nofill3
	s_waitcnt vmcnt(30)
	ds_write_b128 v223, v[4:7]
	ds_write_b128 v223, v[8:11] offset:4608
	ds_write_b128 v223, v[12:15] offset:9216
	ds_write_b128 v223, v[16:19] offset:13824
	ds_write_b128 v223, v[20:23] offset:18432
	ds_write_b128 v223, v[24:27] offset:23040
	ds_write_b128 v223, v[28:31] offset:27648
	ds_write_b128 v223, v[32:35] offset:32256
	ds_write_b128 v193, v[36:39] offset:36864
	ds_write_b128 v193, v[40:43] offset:40960
	s_and_saveexec_b64 s[42:43], s[38:39]
	s_cbranch_execz .Lg4_fa8
	ds_write_b32 v213, v44 offset:45056
.Lg4_fa8:
	s_or_b64 exec, exec, s[42:43]
	s_and_saveexec_b64 s[42:43], s[40:41]
	s_cbranch_execz .Lg4_fb8
	ds_write_b32 v3, v45 offset:45568

; #define LDS_BARRIER() asm volatile("s_waitcnt lgkmcnt(0)\n\ts_barrier" ::: "memory")
; __device__ void phase_gdn_chain(const Params& p, int l, char* smem, int vb, int nvb, int oz) {
;     ...
;             for (int ci = 0; ci < 36; ci += 6) {
;                 GDN_FILL(rb, vb_, gb, 1)  if (ci + 4 < 36) GDN_LOAD(rb, vb_, gb, ci + 4)  LDS_BARRIER();
;                 GDN_FILL(rc, vc_, gc, 0)  if (ci + 5 < 36) GDN_LOAD(rc, vc_, gc, ci + 5)  LDS_BARRIER();
;                 GDN_FILL(ra, va, ga, 1)  if (ci + 6 < 36) GDN_LOAD(ra, va, ga, ci + 6)  LDS_BARRIER();
;                 GDN_FILL(rb, vb_, gb, 0)  if (ci + 7 < 36) GDN_LOAD(rb, vb_, gb, ci + 7)  LDS_BARRIER();
;                 GDN_FILL(rc, vc_, gc, 1)  if (ci + 8 < 36) GDN_LOAD(rc, vc_, gc, ci + 8)  LDS_BARRIER();
;                 if (ci + 6 < 36) GDN_FILL(ra, va, ga, 0)  if (ci + 9 < 36) GDN_LOAD(ra, va, ga, ci + 9)  LDS_BARRIER();
;             }
.Lg4_nofill3:
	s_cmp_gt_u32 s3, 27
	s_cbranch_scc1 .Lg4_nold_3
	s_add_i32 s25, s3, 8
	s_sub_i32 s31, 31, s3
	s_and_b64 s[26:27], s[44:45], exec
	s_cselect_b32 s25, s25, s31
	s_add_i32 s26, s25, s2
	s_ashr_i32 s27, s26, 31
	s_add_u32 s42, s26, s84
	s_addc_u32 s43, s27, 0
	s_lshl_b64 s[46:47], s[42:43], 13
	s_add_u32 s48, s4, s46
	s_addc_u32 s49, s5, s47
	s_add_u32 s50, s6, s46
	s_addc_u32 s51, s7, s47
	s_lshl_b64 s[26:27], s[26:27], 13
	s_add_u32 s52, s8, s26
	s_addc_u32 s53, s9, s27
	s_add_u32 s26, s10, s26
	s_addc_u32 s27, s11, s27
	s_add_u32 s46, s12, s46
	s_addc_u32 s47, s13, s47
	global_load_dwordx4 v[4:7], v2, s[48:49] nt
	global_load_dwordx4 v[12:15], v2, s[50:51] nt
	global_load_dwordx4 v[16:19], v215, s[50:51] nt
	global_load_dwordx4 v[24:27], v215, s[52:53] nt
	global_load_dwordx4 v[20:23], v2, s[52:53] nt
	global_load_dwordx4 v[28:31], v2, s[26:27] nt
	global_load_dwordx4 v[8:11], v215, s[48:49] nt
	global_load_dwordx4 v[36:39], v2, s[46:47] nt
	global_load_dwordx4 v[32:35], v215, s[26:27] nt
	global_load_dwordx4 v[40:43], v215, s[46:47] nt
	s_lshl_b64 s[26:27], s[42:43], 10
	s_add_u32 s42, s14, s26
	s_addc_u32 s43, s15, s27
	s_and_saveexec_b64 s[46:47], s[38:39]
	s_cbranch_execz .Lg4_la9
	global_load_dword v44, v216, s[42:43]

; #define LDS_BARRIER() asm volatile("s_waitcnt lgkmcnt(0)\n\ts_barrier" ::: "memory")
; __device__ void phase_gdn_chain(const Params& p, int l, char* smem, int vb, int nvb, int oz) {
;     ...
;             for (int ci = 0; ci < 36; ci += 6) {
;                 GDN_FILL(rb, vb_, gb, 1)  if (ci + 4 < 36) GDN_LOAD(rb, vb_, gb, ci + 4)  LDS_BARRIER();
;                 GDN_FILL(rc, vc_, gc, 0)  if (ci + 5 < 36) GDN_LOAD(rc, vc_, gc, ci + 5)  LDS_BARRIER();
;                 GDN_FILL(ra, va, ga, 1)  if (ci + 6 < 36) GDN_LOAD(ra, va, ga, ci + 6)  LDS_BARRIER();
;                 GDN_FILL(rb, vb_, gb, 0)  if (ci + 7 < 36) GDN_LOAD(rb, vb_, gb, ci + 7)  LDS_BARRIER();
;                 GDN_FILL(rc, vc_, gc, 1)  if (ci + 8 < 36) GDN_LOAD(rc, vc_, gc, ci + 8)  LDS_BARRIER();
;                 if (ci + 6 < 36) GDN_FILL(ra, va, ga, 0)  if (ci + 9 < 36) GDN_LOAD(ra, va, ga, ci + 9)  LDS_BARRIER();
;             }
.Lg4_nold_3:
	s_waitcnt lgkmcnt(0)
	s_barrier
	s_add_i32 s3, s3, 4
	s_cmp_lt_u32 s3, 36
	s_cbranch_scc1 .Lg4_loop
	s_branch .LBB0_389
